# v11
# baseline (speedup 1.0000x reference)
_Z9nerf_mainPKfS0_S0_PKiS2_PKcS0_Pf:
	s_load_dwordx8 s[8:15], s[0:1], 0x20
	s_load_dwordx8 s[24:31], s[0:1], 0x0
	v_readfirstlane_b32 s3, v0
	v_and_b32_e32 v120, 63, v0
	v_lshlrev_b32_e32 v121, 4, v120
	s_mov_b32 s39, 0x20000
	s_waitcnt lgkmcnt(0)
	s_load_dword s50, s[30:31], 0x0
	s_load_dword s51, s[8:9], 0x0
	s_load_dwordx8 s[52:59], s[28:29], 0x0
	s_load_dwordx4 s[60:63], s[28:29], 0x20
	s_lshr_b32 s64, s3, 7
	s_lshl_b32 s65, s2, 2
	s_add_i32 s64, s64, s65
	s_ashr_i32 s65, s64, 31
	s_lshl_b64 s[64:65], s[64:65], 2
	s_add_u32 s66, s24, s64
	s_addc_u32 s67, s25, s65
	s_add_u32 s64, s26, s64
	s_addc_u32 s65, s27, s65
	s_load_dword s68, s[66:67], 0x0
	s_load_dword s69, s[64:65], 0x0
	v_lshlrev_b32_e32 v188, 2, v0
	v_add_u32_e32 v189, 0x1000, v188
	global_load_dword v184, v188, s[12:13]
	global_load_dword v185, v188, s[12:13] offset:2048
	global_load_dword v186, v189, s[12:13]
	global_load_dword v187, v189, s[12:13] offset:2048
	s_and_b32 s37, s11, 0xffff
	s_lshl_b32 s11, s3, 4
	s_mov_b32 s38, 0xf0000
	s_and_b32 s42, s11, 0xfffffc00
	s_mov_b32 s4, s10
	s_mov_b32 s5, s37
	s_mov_b32 s6, s38
	s_mov_b32 s7, s39
	v_or_b32_e32 v125, s42, v121
	s_add_i32 m0, s42, 0x1a000
	s_movk_i32 s11, 0x2000
	buffer_load_dwordx4 v125, s[4:7], 0 offen lds
	s_add_i32 m0, s42, 0x1c000
	s_nop 0
	buffer_load_dwordx4 v125, s[4:7], s11 offen lds
	s_add_i32 m0, s42, 0x1e000
	s_movk_i32 s11, 0x4000
	buffer_load_dwordx4 v125, s[4:7], s11 offen lds
	s_add_i32 m0, s42, 0x20000
	s_movk_i32 s11, 0x6000
	buffer_load_dwordx4 v125, s[4:7], s11 offen lds
	s_add_i32 m0, s42, 0x22000
	s_mov_b32 s11, 0xe8000
	buffer_load_dwordx4 v125, s[4:7], s11 offen lds
	s_lshr_b32 s70, s2, 3
	s_cmp_ge_u32 s70, 30
	s_cselect_b32 s71, 30, 0
	s_sub_u32 s70, s70, s71
	s_lshl_b32 s70, s70, 15
	v_lshlrev_b32_e32 v190, 4, v0
	buffer_load_dwordx4 v[192:195], v190, s[4:7], s70 offen
	s_add_u32 s71, s70, 0x2000
	buffer_load_dwordx4 v[196:199], v190, s[4:7], s71 offen
	s_add_u32 s72, s70, 0x4000
	buffer_load_dwordx4 v[200:203], v190, s[4:7], s72 offen
	s_add_u32 s73, s70, 0x6000
	buffer_load_dwordx4 v[204:207], v190, s[4:7], s73 offen
	s_mov_b32 s36, s10
	s_waitcnt lgkmcnt(0)
	s_mov_b32 s0, s50
	s_lshl_b32 s1, s2, 2
	s_mov_b32 s2, s51
	s_lshr_b32 s31, s3, 7
	s_bfe_u32 s30, s3, 0x10006
	s_waitcnt lgkmcnt(0)
	v_cvt_f32_i32_e32 v1, s0
	s_add_i32 s12, s31, s1
	s_add_i32 s1, s0, 0xf423f
	s_cmp_lt_u32 s1, 0x1e847f
	v_mov_b32_e32 v2, s0
	s_cselect_b64 vcc, -1, 0
	v_cndmask_b32_e32 v123, v2, v1, vcc
	v_cvt_f32_i32_e32 v1, s2
	s_add_i32 s0, s2, 0xf423f
	s_cmp_lt_u32 s0, 0x1e847f
	v_mov_b32_e32 v2, s2
	s_cselect_b64 vcc, -1, 0
	v_cndmask_b32_e32 v1, v2, v1, vcc
	v_sub_f32_e32 v122, v1, v123
	s_mov_b32 s2, 0x427c0000
	v_div_scale_f32 v1, s[0:1], s2, s2, v122
	v_rcp_f32_e32 v2, v1
	s_ashr_i32 s13, s12, 31
	s_lshl_b64 s[0:1], s[12:13], 2
	s_add_u32 s4, s24, s0
	v_fma_f32 v5, -v1, v2, 1.0
	s_addc_u32 s5, s25, s1
	v_fmac_f32_e32 v2, v5, v2
	v_div_scale_f32 v5, vcc, v122, s2, v122
	s_add_u32 s0, s26, s0
	v_mul_f32_e32 v6, v5, v2
	s_mov_b64 s[16:17], s[52:53]
	s_mov_b64 s[18:19], s[54:55]
	s_mov_b64 s[20:21], s[56:57]
	s_mov_b64 s[22:23], s[58:59]
	s_addc_u32 s1, s27, s1
	v_fma_f32 v7, -v1, v6, v5
	s_mov_b32 s4, s68
	v_fmac_f32_e32 v6, v7, v2
	s_mov_b32 s0, s69
	v_fma_f32 v1, -v1, v6, v5
	v_div_fmas_f32 v1, v1, v2, v6
	v_div_fixup_f32 v124, v1, s2, v122
	s_waitcnt lgkmcnt(0)
	v_mov_b32_e32 v1, s16
	s_mov_b64 s[24:25], s[60:61]
	s_mov_b64 s[26:27], s[62:63]
	v_mul_f32_e32 v1, s4, v1
	v_mov_b32_e32 v2, s0
	v_fma_f32 v1, s17, -v2, v1
	v_add_f32_e32 v127, s19, v1
	v_mov_b32_e32 v1, s20
	v_mul_f32_e32 v1, s4, v1
	v_fma_f32 v1, s21, -v2, v1
	v_add_f32_e32 v128, s23, v1
	s_waitcnt lgkmcnt(0)
	v_mov_b32_e32 v1, s24
	v_mul_f32_e32 v1, s4, v1
	v_and_b32_e32 v3, 15, v0
	v_fma_f32 v1, s25, -v2, v1
	v_and_b32_e32 v131, 48, v0
	v_lshl_or_b32 v0, s30, 6, v120
	v_add_f32_e32 v129, s27, v1
	v_add_u32_e32 v1, 1, v0
	v_cvt_f32_ubyte0_e32 v1, v1
	s_mov_b32 s4, 0x43010000
	s_and_b32 s19, s3, 0xffffff80
	v_div_scale_f32 v2, s[2:3], s4, s4, v1
	v_lshl_or_b32 v130, s30, 5, v3
	v_rcp_f32_e32 v3, v2
	v_lshrrev_b32_e32 v4, 4, v120
	v_cmp_eq_u32_e64 s[8:9], 2, v4
	v_cmp_eq_u32_e64 s[10:11], 1, v4
	v_fma_f32 v5, -v2, v3, 1.0
	v_fmac_f32_e32 v3, v5, v3
	v_div_scale_f32 v5, vcc, v1, s4, v1
	v_mul_f32_e32 v6, v5, v3
	v_fma_f32 v7, -v2, v6, v5
	v_fmac_f32_e32 v6, v7, v3
	v_fma_f32 v2, -v2, v6, v5
	v_div_fmas_f32 v2, v2, v3, v6
	v_div_fixup_f32 v134, v2, s4, v1
	v_add_u32_e32 v2, -1, v4
	v_cmp_gt_u32_e32 vcc, 2, v2
	v_mov_b32_e32 v2, 0x401550d3
	v_mov_b32_e32 v3, 0x436d0620
	v_cndmask_b32_e64 v5, v2, v3, s[8:9]
	v_mov_b32_e32 v6, 0x412e2e5e
	v_cmp_eq_u32_e64 s[0:1], 3, v4
	v_cndmask_b32_e64 v4, v5, v6, s[10:11]
	v_cmp_gt_u32_e64 s[2:3], 16, v120
	v_bfrev_b32_e32 v5, 34
	v_mov_b32_e32 v8, 0x41bc2043
	v_cndmask_b32_e64 v140, v4, 0.5, s[2:3]
	v_mov_b32_e32 v4, 0x40a14518
	v_cndmask_b32_e64 v7, v4, v5, s[8:9]
	v_cndmask_b32_e64 v7, v7, v8, s[10:11]
	v_mov_b32_e32 v9, 0x3f8a3f66
	v_cndmask_b32_e64 v141, v7, v9, s[2:3]
	v_cndmask_b32_e64 v7, v6, 0.5, s[8:9]
	v_cndmask_b32_e64 v6, v3, v6, s[8:9]
	v_mov_b32_e32 v10, 0x424b2ff5
	v_cndmask_b32_e64 v6, v6, 0.5, s[10:11]
	v_cndmask_b32_e64 v144, v6, v10, s[2:3]
	v_cndmask_b32_e64 v6, v5, v8, s[8:9]
	v_or_b32_e32 v0, s19, v0
	v_mov_b32_e32 v11, 0x42db7457
	v_cndmask_b32_e64 v6, v6, v9, s[10:11]
	v_lshlrev_b32_e32 v0, 2, v0
	v_cndmask_b32_e64 v7, v7, v10, s[10:11]
	v_cndmask_b32_e64 v145, v6, v11, s[2:3]
	v_cndmask_b32_e64 v6, 0, v10, s[8:9]
	v_add_u32_e32 v135, 0x15000, v0
	v_add_u32_e32 v136, 0x15800, v0
	v_cvt_f32_ubyte0_e32 v0, v130
	v_or_b32_e32 v138, 16, v130
	v_cndmask_b32_e64 v142, v7, v2, s[2:3]
	v_cndmask_b32_e64 v2, v6, v2, s[10:11]
	s_lshl_b32 s13, s31, 10
	s_lshl_b32 s44, s31, 8
	v_fma_f32 v137, v0, v124, v123
	v_cvt_f32_ubyte0_e32 v0, v138
	v_cndmask_b32_e64 v7, v8, v9, s[8:9]
	v_cndmask_b32_e64 v146, v2, v3, s[2:3]
	v_cndmask_b32_e64 v2, 0, v11, s[8:9]
	s_lshl_b32 s27, s19, 2
	s_add_i32 s13, s13, 0x12000
	s_add_i32 s44, s44, 0x16000
	v_fma_f32 v139, v0, v124, v123
	v_lshlrev_b32_e32 v0, 4, v130
	v_lshlrev_b32_e32 v1, 4, v138
	v_cndmask_b32_e64 v7, v7, v11, s[10:11]
	v_cndmask_b32_e64 v2, v2, v4, s[10:11]
	v_or_b32_e32 v126, 0x2000, v121
	s_add_i32 s23, s27, 0x15000
	s_add_i32 s28, s42, 0xa000
	s_add_i32 s29, s42, 0xc000
	s_add_i32 s33, s42, 0xe000
	s_add_i32 s34, s42, 0x10000
	s_add_i32 s35, s42, 0x2000
	s_add_i32 s40, s42, 0x8000
	s_add_i32 s41, s42, 0x6000
	s_addk_i32 s42, 0x4000
	s_sub_i32 s43, s19, 64
	v_lshl_or_b32 v132, v120, 4, s13
	v_lshl_or_b32 v133, v120, 2, s44
	s_mov_b32 s20, 1
	s_or_b64 s[4:5], s[2:3], vcc
	s_or_b64 s[6:7], s[2:3], s[10:11]
	v_cndmask_b32_e64 v143, v7, v4, s[2:3]
	s_mov_b32 s45, 0
	v_cndmask_b32_e64 v147, v2, v5, s[2:3]
	v_or_b32_e32 v148, 0x1a000, v121
	v_or_b32_e32 v149, 0x1a400, v121
	v_or_b32_e32 v150, 0x1a800, v121
	v_or_b32_e32 v151, 0x1ac00, v121
	v_or_b32_e32 v152, 0x1b000, v121
	v_or_b32_e32 v153, 0x1b400, v121
	v_or_b32_e32 v154, 0x1b800, v121
	v_or_b32_e32 v155, 0x1bc00, v121
	v_or_b32_e32 v156, 0x1c000, v121
	v_or_b32_e32 v157, 0x1c400, v121
	v_or_b32_e32 v158, 0x1c800, v121
	v_or_b32_e32 v159, 0x1cc00, v121
	v_or_b32_e32 v160, 0x1d000, v121
	v_or_b32_e32 v161, 0x1d400, v121
	v_or_b32_e32 v162, 0x1d800, v121
	v_or_b32_e32 v163, 0x1dc00, v121
	v_or_b32_e32 v164, 0x1e000, v121
	v_or_b32_e32 v165, 0x1e400, v121
	v_or_b32_e32 v166, 0x1e800, v121
	v_or_b32_e32 v167, 0x1ec00, v121
	v_or_b32_e32 v168, 0x1f000, v121
	v_or_b32_e32 v169, 0x1f400, v121
	v_or_b32_e32 v170, 0x1f800, v121
	v_or_b32_e32 v171, 0x1fc00, v121
	v_or_b32_e32 v172, 0x20000, v121
	v_or_b32_e32 v173, 0x20400, v121
	v_or_b32_e32 v174, 0x20800, v121
	v_or_b32_e32 v175, 0x20c00, v121
	v_or_b32_e32 v176, 0x21000, v121
	v_or_b32_e32 v177, 0x21400, v121
	v_or_b32_e32 v178, 0x21800, v121
	v_or_b32_e32 v179, 0x21c00, v121
	v_add_u32_e32 v180, s13, v0
	v_add_u32_e32 v181, s13, v1
	v_mov_b32_e32 v182, 0x13000
	s_waitcnt vmcnt(9)
	ds_write_b32 v188, v184
	ds_write_b32 v188, v185 offset:2048
	ds_write_b32 v188, v186 offset:4096
	ds_write_b32 v188, v187 offset:6144
	s_branch .LBB1_5
